# pooling phase: initial window-sum loop fetches 8 rows per trip instead of one serialized load per iteration
# speedup vs baseline: 1.0164x; 1.0072x over previous
.LBB0_1166:
	s_mov_b64 s[100:101], exec
	v_sub_u32_e32 v245, v107, v8
	v_add_u32_e32 v245, -1, v245
	global_load_dwordx4 v[212:215], v[6:7], off
	v_min_u32_e32 v244, 1, v245
	v_mad_u64_u32 v[246:247], s[98:99], v244, s14, v[6:7]
	global_load_dwordx4 v[216:219], v[246:247], off
	v_min_u32_e32 v244, 2, v245
	v_mad_u64_u32 v[246:247], s[98:99], v244, s14, v[6:7]
	global_load_dwordx4 v[220:223], v[246:247], off
	v_min_u32_e32 v244, 3, v245
	v_mad_u64_u32 v[246:247], s[98:99], v244, s14, v[6:7]
	global_load_dwordx4 v[224:227], v[246:247], off
	v_min_u32_e32 v244, 4, v245
	v_mad_u64_u32 v[246:247], s[98:99], v244, s14, v[6:7]
	global_load_dwordx4 v[228:231], v[246:247], off
	v_min_u32_e32 v244, 5, v245
	v_mad_u64_u32 v[246:247], s[98:99], v244, s14, v[6:7]
	global_load_dwordx4 v[232:235], v[246:247], off
	v_min_u32_e32 v244, 6, v245
	v_mad_u64_u32 v[246:247], s[98:99], v244, s14, v[6:7]
	global_load_dwordx4 v[236:239], v[246:247], off
	v_min_u32_e32 v244, 7, v245
	v_mad_u64_u32 v[246:247], s[98:99], v244, s14, v[6:7]
	global_load_dwordx4 v[240:243], v[246:247], off
	s_waitcnt vmcnt(7)
	v_lshlrev_b32_e32 v248, 16, v212
	v_and_b32_e32 v249, 0xffff0000, v212
	v_pk_add_f32 v[118:119], v[118:119], v[248:249]
	v_lshlrev_b32_e32 v248, 16, v213
	v_and_b32_e32 v249, 0xffff0000, v213
	v_pk_add_f32 v[116:117], v[116:117], v[248:249]
	v_lshlrev_b32_e32 v248, 16, v214
	v_and_b32_e32 v249, 0xffff0000, v214
	v_pk_add_f32 v[110:111], v[110:111], v[248:249]
	v_lshlrev_b32_e32 v248, 16, v215
	v_and_b32_e32 v249, 0xffff0000, v215
	v_pk_add_f32 v[108:109], v[108:109], v[248:249]
	v_cmp_le_u32_e32 vcc, 1, v245
	s_nop 1
	s_and_b64 exec, exec, vcc
	s_waitcnt vmcnt(6)
	v_lshlrev_b32_e32 v248, 16, v216
	v_and_b32_e32 v249, 0xffff0000, v216
	v_pk_add_f32 v[118:119], v[118:119], v[248:249]
	v_lshlrev_b32_e32 v248, 16, v217
	v_and_b32_e32 v249, 0xffff0000, v217
	v_pk_add_f32 v[116:117], v[116:117], v[248:249]
	v_lshlrev_b32_e32 v248, 16, v218
	v_and_b32_e32 v249, 0xffff0000, v218
	v_pk_add_f32 v[110:111], v[110:111], v[248:249]
	v_lshlrev_b32_e32 v248, 16, v219
	v_and_b32_e32 v249, 0xffff0000, v219
	v_pk_add_f32 v[108:109], v[108:109], v[248:249]
	v_cmp_le_u32_e32 vcc, 2, v245
	s_nop 1
	s_and_b64 exec, exec, vcc
	s_waitcnt vmcnt(5)
	v_lshlrev_b32_e32 v248, 16, v220
	v_and_b32_e32 v249, 0xffff0000, v220
	v_pk_add_f32 v[118:119], v[118:119], v[248:249]
	v_lshlrev_b32_e32 v248, 16, v221
	v_and_b32_e32 v249, 0xffff0000, v221
	v_pk_add_f32 v[116:117], v[116:117], v[248:249]
	v_lshlrev_b32_e32 v248, 16, v222
	v_and_b32_e32 v249, 0xffff0000, v222
	v_pk_add_f32 v[110:111], v[110:111], v[248:249]
	v_lshlrev_b32_e32 v248, 16, v223
	v_and_b32_e32 v249, 0xffff0000, v223
	v_pk_add_f32 v[108:109], v[108:109], v[248:249]
	v_cmp_le_u32_e32 vcc, 3, v245
	s_nop 1
	s_and_b64 exec, exec, vcc
	s_waitcnt vmcnt(4)
	v_lshlrev_b32_e32 v248, 16, v224
	v_and_b32_e32 v249, 0xffff0000, v224
	v_pk_add_f32 v[118:119], v[118:119], v[248:249]
	v_lshlrev_b32_e32 v248, 16, v225
	v_and_b32_e32 v249, 0xffff0000, v225
	v_pk_add_f32 v[116:117], v[116:117], v[248:249]
	v_lshlrev_b32_e32 v248, 16, v226
	v_and_b32_e32 v249, 0xffff0000, v226
	v_pk_add_f32 v[110:111], v[110:111], v[248:249]
	v_lshlrev_b32_e32 v248, 16, v227
	v_and_b32_e32 v249, 0xffff0000, v227
	v_pk_add_f32 v[108:109], v[108:109], v[248:249]
	v_cmp_le_u32_e32 vcc, 4, v245
	s_nop 1
	s_and_b64 exec, exec, vcc
	s_waitcnt vmcnt(3)
	v_lshlrev_b32_e32 v248, 16, v228
	v_and_b32_e32 v249, 0xffff0000, v228
	v_pk_add_f32 v[118:119], v[118:119], v[248:249]
	v_lshlrev_b32_e32 v248, 16, v229
	v_and_b32_e32 v249, 0xffff0000, v229
	v_pk_add_f32 v[116:117], v[116:117], v[248:249]
	v_lshlrev_b32_e32 v248, 16, v230
	v_and_b32_e32 v249, 0xffff0000, v230
	v_pk_add_f32 v[110:111], v[110:111], v[248:249]
	v_lshlrev_b32_e32 v248, 16, v231
	v_and_b32_e32 v249, 0xffff0000, v231
	v_pk_add_f32 v[108:109], v[108:109], v[248:249]
	v_cmp_le_u32_e32 vcc, 5, v245
	s_nop 1
	s_and_b64 exec, exec, vcc
	s_waitcnt vmcnt(2)
	v_lshlrev_b32_e32 v248, 16, v232
	v_and_b32_e32 v249, 0xffff0000, v232
	v_pk_add_f32 v[118:119], v[118:119], v[248:249]
	v_lshlrev_b32_e32 v248, 16, v233
	v_and_b32_e32 v249, 0xffff0000, v233
	v_pk_add_f32 v[116:117], v[116:117], v[248:249]
	v_lshlrev_b32_e32 v248, 16, v234
	v_and_b32_e32 v249, 0xffff0000, v234
	v_pk_add_f32 v[110:111], v[110:111], v[248:249]
	v_lshlrev_b32_e32 v248, 16, v235
	v_and_b32_e32 v249, 0xffff0000, v235
	v_pk_add_f32 v[108:109], v[108:109], v[248:249]
	v_cmp_le_u32_e32 vcc, 6, v245
	s_nop 1
	s_and_b64 exec, exec, vcc
	s_waitcnt vmcnt(1)
	v_lshlrev_b32_e32 v248, 16, v236
	v_and_b32_e32 v249, 0xffff0000, v236
	v_pk_add_f32 v[118:119], v[118:119], v[248:249]
	v_lshlrev_b32_e32 v248, 16, v237
	v_and_b32_e32 v249, 0xffff0000, v237
	v_pk_add_f32 v[116:117], v[116:117], v[248:249]
	v_lshlrev_b32_e32 v248, 16, v238
	v_and_b32_e32 v249, 0xffff0000, v238
	v_pk_add_f32 v[110:111], v[110:111], v[248:249]
	v_lshlrev_b32_e32 v248, 16, v239
	v_and_b32_e32 v249, 0xffff0000, v239
	v_pk_add_f32 v[108:109], v[108:109], v[248:249]
	v_cmp_le_u32_e32 vcc, 7, v245
	s_nop 1
	s_and_b64 exec, exec, vcc
	s_waitcnt vmcnt(0)
	v_lshlrev_b32_e32 v248, 16, v240
	v_and_b32_e32 v249, 0xffff0000, v240
	v_pk_add_f32 v[118:119], v[118:119], v[248:249]
	v_lshlrev_b32_e32 v248, 16, v241
	v_and_b32_e32 v249, 0xffff0000, v241
	v_pk_add_f32 v[116:117], v[116:117], v[248:249]
	v_lshlrev_b32_e32 v248, 16, v242
	v_and_b32_e32 v249, 0xffff0000, v242
	v_pk_add_f32 v[110:111], v[110:111], v[248:249]
	v_lshlrev_b32_e32 v248, 16, v243
	v_and_b32_e32 v249, 0xffff0000, v243
	v_pk_add_f32 v[108:109], v[108:109], v[248:249]
	s_mov_b64 exec, s[100:101]
	v_add_u32_e32 v8, 8, v8
	s_lshl_b64 s[98:99], s[14:15], 3
	v_lshl_add_u64 v[6:7], v[6:7], 0, s[98:99]
	v_cmp_ge_u32_e32 vcc, v8, v107
	s_nop 1
	s_or_b64 s[26:27], vcc, s[26:27]
	s_andn2_b64 exec, exec, s[26:27]
	s_cbranch_execnz .LBB0_1166
	s_or_b64 exec, exec, s[26:27]
